# baseline (speedup 1.0000x reference)
.LBB3_16:
	s_or_b64 exec, exec, s[2:3]
	s_ashr_i32 s29, s24, 7
	s_mul_i32 s27, s29, 0x3f48000
	s_mul_hi_i32 s26, s29, 0x3f48000
	s_add_u32 s24, s12, s27
	s_addc_u32 s25, s13, s26
	v_cmp_ne_u32_e64 s[0:1], -2, v4
	v_cmp_ne_u32_e64 s[2:3], -2, v2
	v_cmp_ne_u32_e64 s[4:5], -2, v6
	s_mov_b32 s63, 0x38800000
	s_mov_b64 s[44:45], s[24:25]
	s_add_u32 s46, s24, 0x1fa40
	s_addc_u32 s47, s25, 0
	s_add_u32 s48, s24, 0x3f480
	s_addc_u32 s49, s25, 0
	s_add_u32 s50, s24, 0x5eec0
	s_addc_u32 s51, s25, 0
	s_add_u32 s52, s24, 0x7e900
	s_addc_u32 s53, s25, 0
	s_add_u32 s54, s24, 0x9e340
	s_addc_u32 s55, s25, 0
	s_add_u32 s56, s24, 0xbdd80
	s_addc_u32 s57, s25, 0
	s_add_u32 s58, s24, 0xdd7c0
	s_addc_u32 s59, s25, 0
	v_lshlrev_b32_e32 v224, 2, v4
	v_lshlrev_b32_e32 v225, 2, v2
	v_lshlrev_b32_e32 v226, 2, v6
	v_mov_b32_e32 v200, 0
	v_mov_b32_e32 v201, 0
	v_mov_b32_e32 v202, 0
	v_mov_b32_e32 v203, 0
	v_mov_b32_e32 v204, 0
	v_mov_b32_e32 v205, 0
	v_mov_b32_e32 v206, 0
	v_mov_b32_e32 v207, 0
	v_mov_b32_e32 v208, 0
	v_mov_b32_e32 v209, 0
	v_mov_b32_e32 v210, 0
	v_mov_b32_e32 v211, 0
	v_mov_b32_e32 v212, 0
	v_mov_b32_e32 v213, 0
	v_mov_b32_e32 v214, 0
	v_mov_b32_e32 v215, 0
	v_mov_b32_e32 v216, 0
	v_mov_b32_e32 v217, 0
	v_mov_b32_e32 v218, 0
	v_mov_b32_e32 v219, 0
	v_mov_b32_e32 v220, 0
	v_mov_b32_e32 v221, 0
	v_mov_b32_e32 v222, 0
	v_mov_b32_e32 v223, 0
	v_cmp_lt_i32_e32 vcc, -1, v4
	s_and_saveexec_b64 s[8:9], vcc
	global_load_dword v200, v224, s[44:45]
	global_load_dword v201, v224, s[46:47]
	global_load_dword v202, v224, s[48:49]
	global_load_dword v203, v224, s[50:51]
	global_load_dword v204, v224, s[52:53]
	global_load_dword v205, v224, s[54:55]
	global_load_dword v206, v224, s[56:57]
	global_load_dword v207, v224, s[58:59]
	s_mov_b64 exec, s[8:9]
	v_cmp_lt_i32_e32 vcc, -1, v2
	s_and_saveexec_b64 s[8:9], vcc
	global_load_dword v208, v225, s[44:45]
	global_load_dword v209, v225, s[46:47]
	global_load_dword v210, v225, s[48:49]
	global_load_dword v211, v225, s[50:51]
	global_load_dword v212, v225, s[52:53]
	global_load_dword v213, v225, s[54:55]
	global_load_dword v214, v225, s[56:57]
	global_load_dword v215, v225, s[58:59]
	s_mov_b64 exec, s[8:9]
	v_cmp_lt_i32_e32 vcc, -1, v6
	s_and_saveexec_b64 s[8:9], vcc
	global_load_dword v216, v226, s[44:45]
	global_load_dword v217, v226, s[46:47]
	global_load_dword v218, v226, s[48:49]
	global_load_dword v219, v226, s[50:51]
	global_load_dword v220, v226, s[52:53]
	global_load_dword v221, v226, s[54:55]
	global_load_dword v222, v226, s[56:57]
	global_load_dword v223, v226, s[58:59]
	s_mov_b64 exec, s[8:9]
	s_waitcnt vmcnt(0)
	v_cvt_f16_f32_e32 v250, v200
	v_cvt_f16_f32_e32 v251, v201
	v_cvt_f32_f16_e32 v254, v250
	v_cvt_f32_f16_e32 v255, v251
	v_cmp_lt_f32_e64 s[36:37], |v254|, s63
	v_cmp_lt_f32_e64 s[38:39], |v255|, s63
	s_nop 0
	v_cndmask_b32_e64 v254, v254, 0, s[36:37]
	v_cndmask_b32_e64 v250, v250, 0, s[36:37]
	v_cndmask_b32_e64 v255, v255, 0, s[38:39]
	v_cndmask_b32_e64 v251, v251, 0, s[38:39]
	v_sub_f32_e32 v200, v200, v254
	v_sub_f32_e32 v201, v201, v255
	v_mul_f32_e32 v200, 0x45000000, v200
	v_mul_f32_e32 v201, 0x45000000, v201
	v_pack_b32_f16 v248, v250, v251
	v_cvt_pk_f16_f32 v252, v200, v201
	v_cvt_f16_f32_e32 v250, v202
	v_cvt_f16_f32_e32 v251, v203
	v_cvt_f32_f16_e32 v254, v250
	v_cvt_f32_f16_e32 v255, v251
	v_cmp_lt_f32_e64 s[36:37], |v254|, s63
	v_cmp_lt_f32_e64 s[38:39], |v255|, s63
	s_nop 0
	v_cndmask_b32_e64 v254, v254, 0, s[36:37]
	v_cndmask_b32_e64 v250, v250, 0, s[36:37]
	v_cndmask_b32_e64 v255, v255, 0, s[38:39]
	v_cndmask_b32_e64 v251, v251, 0, s[38:39]
	v_sub_f32_e32 v202, v202, v254
	v_sub_f32_e32 v203, v203, v255
	v_mul_f32_e32 v202, 0x45000000, v202
	v_mul_f32_e32 v203, 0x45000000, v203
	v_pack_b32_f16 v249, v250, v251
	v_cvt_pk_f16_f32 v253, v202, v203
	v_cvt_f16_f32_e32 v200, v204
	v_cvt_f16_f32_e32 v201, v205
	v_cvt_f32_f16_e32 v202, v200
	v_cvt_f32_f16_e32 v203, v201
	v_cmp_lt_f32_e64 s[36:37], |v202|, s63
	v_cmp_lt_f32_e64 s[38:39], |v203|, s63
	s_nop 0
	v_cndmask_b32_e64 v202, v202, 0, s[36:37]
	v_cndmask_b32_e64 v200, v200, 0, s[36:37]
	v_cndmask_b32_e64 v203, v203, 0, s[38:39]
	v_cndmask_b32_e64 v201, v201, 0, s[38:39]
	v_sub_f32_e32 v204, v204, v202
	v_sub_f32_e32 v205, v205, v203
	v_mul_f32_e32 v204, 0x45000000, v204
	v_mul_f32_e32 v205, 0x45000000, v205
	v_pack_b32_f16 v250, v200, v201
	v_cvt_pk_f16_f32 v254, v204, v205
	v_cvt_f16_f32_e32 v200, v206
	v_cvt_f16_f32_e32 v201, v207
	v_cvt_f32_f16_e32 v202, v200
	v_cvt_f32_f16_e32 v203, v201
	v_cmp_lt_f32_e64 s[36:37], |v202|, s63
	v_cmp_lt_f32_e64 s[38:39], |v203|, s63
	s_nop 0
	v_cndmask_b32_e64 v202, v202, 0, s[36:37]
	v_cndmask_b32_e64 v200, v200, 0, s[36:37]
	v_cndmask_b32_e64 v203, v203, 0, s[38:39]
	v_cndmask_b32_e64 v201, v201, 0, s[38:39]
	v_sub_f32_e32 v206, v206, v202
	v_sub_f32_e32 v207, v207, v203
	v_mul_f32_e32 v206, 0x45000000, v206
	v_mul_f32_e32 v207, 0x45000000, v207
	v_pack_b32_f16 v251, v200, v201
	v_cvt_pk_f16_f32 v255, v206, v207
	v_lshlrev_b32_e32 v228, 4, v152
	v_lshlrev_b32_e32 v229, 4, v1
	s_and_saveexec_b64 s[8:9], s[0:1]
	ds_write_b128 v228, v[248:251]
	ds_write_b128 v229, v[252:255]
	s_mov_b64 exec, s[8:9]
	v_cvt_f16_f32_e32 v250, v208
	v_cvt_f16_f32_e32 v251, v209
	v_cvt_f32_f16_e32 v254, v250
	v_cvt_f32_f16_e32 v255, v251
	v_cmp_lt_f32_e64 s[36:37], |v254|, s63
	v_cmp_lt_f32_e64 s[38:39], |v255|, s63
	s_nop 0
	v_cndmask_b32_e64 v254, v254, 0, s[36:37]
	v_cndmask_b32_e64 v250, v250, 0, s[36:37]
	v_cndmask_b32_e64 v255, v255, 0, s[38:39]
	v_cndmask_b32_e64 v251, v251, 0, s[38:39]
	v_sub_f32_e32 v208, v208, v254
	v_sub_f32_e32 v209, v209, v255
	v_mul_f32_e32 v208, 0x45000000, v208
	v_mul_f32_e32 v209, 0x45000000, v209
	v_pack_b32_f16 v248, v250, v251
	v_cvt_pk_f16_f32 v252, v208, v209
	v_cvt_f16_f32_e32 v250, v210
	v_cvt_f16_f32_e32 v251, v211
	v_cvt_f32_f16_e32 v254, v250
	v_cvt_f32_f16_e32 v255, v251
	v_cmp_lt_f32_e64 s[36:37], |v254|, s63
	v_cmp_lt_f32_e64 s[38:39], |v255|, s63
	s_nop 0
	v_cndmask_b32_e64 v254, v254, 0, s[36:37]
	v_cndmask_b32_e64 v250, v250, 0, s[36:37]
	v_cndmask_b32_e64 v255, v255, 0, s[38:39]
	v_cndmask_b32_e64 v251, v251, 0, s[38:39]
	v_sub_f32_e32 v210, v210, v254
	v_sub_f32_e32 v211, v211, v255
	v_mul_f32_e32 v210, 0x45000000, v210
	v_mul_f32_e32 v211, 0x45000000, v211
	v_pack_b32_f16 v249, v250, v251
	v_cvt_pk_f16_f32 v253, v210, v211
	v_cvt_f16_f32_e32 v208, v212
	v_cvt_f16_f32_e32 v209, v213
	v_cvt_f32_f16_e32 v210, v208
	v_cvt_f32_f16_e32 v211, v209
	v_cmp_lt_f32_e64 s[36:37], |v210|, s63
	v_cmp_lt_f32_e64 s[38:39], |v211|, s63
	s_nop 0
	v_cndmask_b32_e64 v210, v210, 0, s[36:37]
	v_cndmask_b32_e64 v208, v208, 0, s[36:37]
	v_cndmask_b32_e64 v211, v211, 0, s[38:39]
	v_cndmask_b32_e64 v209, v209, 0, s[38:39]
	v_sub_f32_e32 v212, v212, v210
	v_sub_f32_e32 v213, v213, v211
	v_mul_f32_e32 v212, 0x45000000, v212
	v_mul_f32_e32 v213, 0x45000000, v213
	v_pack_b32_f16 v250, v208, v209
	v_cvt_pk_f16_f32 v254, v212, v213
	v_cvt_f16_f32_e32 v208, v214
	v_cvt_f16_f32_e32 v209, v215
	v_cvt_f32_f16_e32 v210, v208
	v_cvt_f32_f16_e32 v211, v209
	v_cmp_lt_f32_e64 s[36:37], |v210|, s63
	v_cmp_lt_f32_e64 s[38:39], |v211|, s63
	s_nop 0
	v_cndmask_b32_e64 v210, v210, 0, s[36:37]
	v_cndmask_b32_e64 v208, v208, 0, s[36:37]
	v_cndmask_b32_e64 v211, v211, 0, s[38:39]
	v_cndmask_b32_e64 v209, v209, 0, s[38:39]
	v_sub_f32_e32 v214, v214, v210
	v_sub_f32_e32 v215, v215, v211
	v_mul_f32_e32 v214, 0x45000000, v214
	v_mul_f32_e32 v215, 0x45000000, v215
	v_pack_b32_f16 v251, v208, v209
	v_cvt_pk_f16_f32 v255, v214, v215
	v_lshlrev_b32_e32 v228, 4, v154
	v_lshlrev_b32_e32 v229, 4, v153
	s_and_saveexec_b64 s[8:9], s[2:3]
	ds_write_b128 v228, v[248:251]
	ds_write_b128 v229, v[252:255]
	s_mov_b64 exec, s[8:9]
	v_cvt_f16_f32_e32 v250, v216
	v_cvt_f16_f32_e32 v251, v217
	v_cvt_f32_f16_e32 v254, v250
	v_cvt_f32_f16_e32 v255, v251
	v_cmp_lt_f32_e64 s[36:37], |v254|, s63
	v_cmp_lt_f32_e64 s[38:39], |v255|, s63
	s_nop 0
	v_cndmask_b32_e64 v254, v254, 0, s[36:37]
	v_cndmask_b32_e64 v250, v250, 0, s[36:37]
	v_cndmask_b32_e64 v255, v255, 0, s[38:39]
	v_cndmask_b32_e64 v251, v251, 0, s[38:39]
	v_sub_f32_e32 v216, v216, v254
	v_sub_f32_e32 v217, v217, v255
	v_mul_f32_e32 v216, 0x45000000, v216
	v_mul_f32_e32 v217, 0x45000000, v217
	v_pack_b32_f16 v248, v250, v251
	v_cvt_pk_f16_f32 v252, v216, v217
	v_cvt_f16_f32_e32 v250, v218
	v_cvt_f16_f32_e32 v251, v219
	v_cvt_f32_f16_e32 v254, v250
	v_cvt_f32_f16_e32 v255, v251
	v_cmp_lt_f32_e64 s[36:37], |v254|, s63
	v_cmp_lt_f32_e64 s[38:39], |v255|, s63
	s_nop 0
	v_cndmask_b32_e64 v254, v254, 0, s[36:37]
	v_cndmask_b32_e64 v250, v250, 0, s[36:37]
	v_cndmask_b32_e64 v255, v255, 0, s[38:39]
	v_cndmask_b32_e64 v251, v251, 0, s[38:39]
	v_sub_f32_e32 v218, v218, v254
	v_sub_f32_e32 v219, v219, v255
	v_mul_f32_e32 v218, 0x45000000, v218
	v_mul_f32_e32 v219, 0x45000000, v219
	v_pack_b32_f16 v249, v250, v251
	v_cvt_pk_f16_f32 v253, v218, v219
	v_cvt_f16_f32_e32 v216, v220
	v_cvt_f16_f32_e32 v217, v221
	v_cvt_f32_f16_e32 v218, v216
	v_cvt_f32_f16_e32 v219, v217
	v_cmp_lt_f32_e64 s[36:37], |v218|, s63
	v_cmp_lt_f32_e64 s[38:39], |v219|, s63
	s_nop 0
	v_cndmask_b32_e64 v218, v218, 0, s[36:37]
	v_cndmask_b32_e64 v216, v216, 0, s[36:37]
	v_cndmask_b32_e64 v219, v219, 0, s[38:39]
	v_cndmask_b32_e64 v217, v217, 0, s[38:39]
	v_sub_f32_e32 v220, v220, v218
	v_sub_f32_e32 v221, v221, v219
	v_mul_f32_e32 v220, 0x45000000, v220
	v_mul_f32_e32 v221, 0x45000000, v221
	v_pack_b32_f16 v250, v216, v217
	v_cvt_pk_f16_f32 v254, v220, v221
	v_cvt_f16_f32_e32 v216, v222
	v_cvt_f16_f32_e32 v217, v223
	v_cvt_f32_f16_e32 v218, v216
	v_cvt_f32_f16_e32 v219, v217
	v_cmp_lt_f32_e64 s[36:37], |v218|, s63
	v_cmp_lt_f32_e64 s[38:39], |v219|, s63
	s_nop 0
	v_cndmask_b32_e64 v218, v218, 0, s[36:37]
	v_cndmask_b32_e64 v216, v216, 0, s[36:37]
	v_cndmask_b32_e64 v219, v219, 0, s[38:39]
	v_cndmask_b32_e64 v217, v217, 0, s[38:39]
	v_sub_f32_e32 v222, v222, v218
	v_sub_f32_e32 v223, v223, v219
	v_mul_f32_e32 v222, 0x45000000, v222
	v_mul_f32_e32 v223, 0x45000000, v223
	v_pack_b32_f16 v251, v216, v217
	v_cvt_pk_f16_f32 v255, v222, v223
	v_lshlrev_b32_e32 v228, 4, v156
	v_lshlrev_b32_e32 v229, 4, v155
	s_and_saveexec_b64 s[8:9], s[4:5]
	ds_write_b128 v228, v[248:251]
	ds_write_b128 v229, v[252:255]
	s_mov_b64 exec, s[8:9]
	s_mov_b64 s[8:9], exec
